# baseline (speedup 1.0000x reference)
_Z11edge_kernelILi64ELb0EEvPKfS1_PKDF16_PKiS5_S1_S1_S1_S1_S1_PDF16_:
	s_load_dwordx16 s[4:19], s[0:1], 0x10
	s_load_dwordx2 s[20:21], s[0:1], 0x50
	v_readfirstlane_b32 s3, v0
	v_bfe_u32 v75, v0, 4, 2
	v_and_b32_e32 v76, 15, v0
	v_and_b32_e32 v78, 63, v0
	s_lshr_b32 s3, s3, 6
	s_lshl_b32 s2, s2, 1
	s_add_i32 s2, s2, s3
	v_lshlrev_b32_e32 v74, 8, v75
	v_lshl_or_b32 v74, v76, 4, v74
	v_lshlrev_b32_e32 v79, 4, v78
	v_lshl_or_b32 v77, v76, 2, v75
	v_lshlrev_b32_e32 v77, 2, v77
	v_lshlrev_b32_e32 v78, 5, v75
	v_lshlrev_b32_e32 v73, 12, v75
	v_lshl_or_b32 v73, v76, 4, v73
	s_lshl_b32 s28, s2, 14
	s_lshl_b32 s29, s2, 14
	s_lshl_b32 s30, s2, 2
	s_lshl_b32 s31, s2, 8
	s_lshl_b32 s33, s3, 10
	s_lshl_b32 s34, s3, 8
	s_addk_i32 s34, 0x4000
	s_waitcnt lgkmcnt(0)
	s_add_u32 s6, s6, s30
	s_addc_u32 s7, s7, 0
	s_add_u32 s8, s8, s30
	s_addc_u32 s9, s9, 0
	s_load_dword s35, s[6:7], 0x0
	s_load_dword s36, s[8:9], 0x0
	s_add_u32 s10, s10, s28
	s_addc_u32 s11, s11, 0
	s_add_u32 s18, s18, s33
	s_addc_u32 s19, s19, 0
	s_add_u32 s14, s14, s29
	s_addc_u32 s15, s15, 0
	s_add_u32 s12, s12, s31
	s_addc_u32 s13, s13, 0
	s_add_u32 s16, s16, s31
	s_addc_u32 s17, s17, 0
	s_waitcnt lgkmcnt(0)
	s_lshl_b32 s36, s36, 7
	s_add_u32 s20, s20, s36
	s_addc_u32 s21, s21, 0
	s_lshl_b32 s37, s35, 7
	s_add_u32 s4, s4, s37
	s_addc_u32 s5, s5, 0
	global_load_dwordx4 v[64:67], v78, s[4:5] nt
	global_load_dwordx4 v[68:71], v78, s[4:5] offset:16 nt
	v_add_u32_e32 v78, s34, v77
	v_lshlrev_b32_e32 v96, 12, v75
	v_lshl_or_b32 v96, v76, 4, v96
	s_cmpk_lt_u32 s2, 0x400
	s_cbranch_scc0 .Le2_wait_gather
	global_load_dwordx4 v[0:3], v96, s[10:11] nt
	global_load_dwordx4 v[4:7], v96, s[10:11] offset:256 nt
	global_load_dwordx4 v[8:11], v96, s[10:11] offset:512 nt
	global_load_dwordx4 v[12:15], v96, s[10:11] offset:768 nt
	global_load_dwordx4 v[16:19], v96, s[10:11] offset:1024 nt
	global_load_dwordx4 v[20:23], v96, s[10:11] offset:1280 nt
	global_load_dwordx4 v[24:27], v96, s[10:11] offset:1536 nt
	global_load_dwordx4 v[28:31], v96, s[10:11] offset:1792 nt
	global_load_dwordx4 v[32:35], v96, s[10:11] offset:2048 nt
	global_load_dwordx4 v[36:39], v96, s[10:11] offset:2304 nt
	global_load_dwordx4 v[40:43], v96, s[10:11] offset:2560 nt
	global_load_dwordx4 v[44:47], v96, s[10:11] offset:2816 nt
	global_load_dwordx4 v[48:51], v96, s[10:11] offset:3072 nt
	global_load_dwordx4 v[52:55], v96, s[10:11] offset:3328 nt
	global_load_dwordx4 v[56:59], v96, s[10:11] offset:3584 nt
	global_load_dwordx4 v[60:63], v96, s[10:11] offset:3840 nt
	s_waitcnt vmcnt(16)
	s_branch .Le2_cvt

.Le2_cvt:
	v_cvt_f32_f16_e32 v80, v64
	v_cvt_f32_f16_sdwa v81, v64 dst_sel:DWORD dst_unused:UNUSED_PAD src0_sel:WORD_1
	v_cvt_f32_f16_e32 v82, v65
	v_cvt_f32_f16_sdwa v83, v65 dst_sel:DWORD dst_unused:UNUSED_PAD src0_sel:WORD_1
	v_cvt_f32_f16_e32 v84, v66
	v_cvt_f32_f16_sdwa v85, v66 dst_sel:DWORD dst_unused:UNUSED_PAD src0_sel:WORD_1
	v_cvt_f32_f16_e32 v86, v67
	v_cvt_f32_f16_sdwa v87, v67 dst_sel:DWORD dst_unused:UNUSED_PAD src0_sel:WORD_1
	v_cvt_f32_f16_e32 v88, v68
	v_cvt_f32_f16_sdwa v89, v68 dst_sel:DWORD dst_unused:UNUSED_PAD src0_sel:WORD_1
	v_cvt_f32_f16_e32 v90, v69
	v_cvt_f32_f16_sdwa v91, v69 dst_sel:DWORD dst_unused:UNUSED_PAD src0_sel:WORD_1
	v_cvt_f32_f16_e32 v92, v70
	v_cvt_f32_f16_sdwa v93, v70 dst_sel:DWORD dst_unused:UNUSED_PAD src0_sel:WORD_1
	v_cvt_f32_f16_e32 v94, v71
	v_cvt_f32_f16_sdwa v95, v71 dst_sel:DWORD dst_unused:UNUSED_PAD src0_sel:WORD_1
	v_max_f32_e32 v80, 0, v80
	v_max_f32_e32 v81, 0, v81
	v_max_f32_e32 v82, 0, v82
	v_max_f32_e32 v83, 0, v83
	v_max_f32_e32 v84, 0, v84
	v_max_f32_e32 v85, 0, v85
	v_max_f32_e32 v86, 0, v86
	v_max_f32_e32 v87, 0, v87
	v_max_f32_e32 v88, 0, v88
	v_max_f32_e32 v89, 0, v89
	v_max_f32_e32 v90, 0, v90
	v_max_f32_e32 v91, 0, v91
	v_max_f32_e32 v92, 0, v92
	v_max_f32_e32 v93, 0, v93
	v_max_f32_e32 v94, 0, v94
	v_max_f32_e32 v95, 0, v95
	v_cmp_neq_f32_e64 s[40:41], 0, v80
	v_cmp_neq_f32_e64 s[42:43], 0, v81
	v_cmp_neq_f32_e64 s[44:45], 0, v82
	v_cmp_neq_f32_e64 s[46:47], 0, v83
	v_cmp_neq_f32_e64 s[48:49], 0, v84
	v_cmp_neq_f32_e64 s[50:51], 0, v85
	v_cmp_neq_f32_e64 s[52:53], 0, v86
	v_cmp_neq_f32_e64 s[54:55], 0, v87
	v_cmp_neq_f32_e64 s[56:57], 0, v88
	v_cmp_neq_f32_e64 s[58:59], 0, v89
	v_cmp_neq_f32_e64 s[60:61], 0, v90
	v_cmp_neq_f32_e64 s[62:63], 0, v91
	v_cmp_neq_f32_e64 s[64:65], 0, v92
	v_cmp_neq_f32_e64 s[66:67], 0, v93
	v_cmp_neq_f32_e64 s[68:69], 0, v94
	v_cmp_neq_f32_e64 s[70:71], 0, v95
	s_cmpk_lt_u32 s2, 0x400
	s_cbranch_scc1 .Le2_w1_issued
	s_mov_b64 exec, s[40:41]
	global_load_dwordx4 v[0:3], v96, s[10:11] nt
	s_mov_b64 exec, s[42:43]
	global_load_dwordx4 v[4:7], v96, s[10:11] offset:256 nt
	s_mov_b64 exec, s[44:45]
	global_load_dwordx4 v[8:11], v96, s[10:11] offset:512 nt
	s_mov_b64 exec, s[46:47]
	global_load_dwordx4 v[12:15], v96, s[10:11] offset:768 nt
	s_mov_b64 exec, s[48:49]
	global_load_dwordx4 v[16:19], v96, s[10:11] offset:1024 nt
	s_mov_b64 exec, s[50:51]
	global_load_dwordx4 v[20:23], v96, s[10:11] offset:1280 nt
	s_mov_b64 exec, s[52:53]
	global_load_dwordx4 v[24:27], v96, s[10:11] offset:1536 nt
	s_mov_b64 exec, s[54:55]
	global_load_dwordx4 v[28:31], v96, s[10:11] offset:1792 nt
	s_mov_b64 exec, s[56:57]
	global_load_dwordx4 v[32:35], v96, s[10:11] offset:2048 nt
	s_mov_b64 exec, s[58:59]
	global_load_dwordx4 v[36:39], v96, s[10:11] offset:2304 nt
	s_mov_b64 exec, s[60:61]
	global_load_dwordx4 v[40:43], v96, s[10:11] offset:2560 nt
	s_mov_b64 exec, s[62:63]
	global_load_dwordx4 v[44:47], v96, s[10:11] offset:2816 nt
	s_mov_b64 exec, s[64:65]
	global_load_dwordx4 v[48:51], v96, s[10:11] offset:3072 nt
	s_mov_b64 exec, s[66:67]
	global_load_dwordx4 v[52:55], v96, s[10:11] offset:3328 nt
	s_mov_b64 exec, s[68:69]
	global_load_dwordx4 v[56:59], v96, s[10:11] offset:3584 nt
	s_mov_b64 exec, s[70:71]
	global_load_dwordx4 v[60:63], v96, s[10:11] offset:3840 nt
